# attention: K-ring DMA behind the 2nd P.V MFMA, V-ring DMA behind the 5th, row-max under the P.V MFMAs (on v11)
# baseline (speedup 1.0000x reference)
; #define ATT_DMAK(tile, slot) do { _Pragma("unroll") for (int i = 0; i < 4; ++i) { const int pc = (wv + 8 * i) < 25 ? (wv + 8 * i) : 24; \
;         __builtin_amdgcn_global_load_lds((const unsigned*)((const char*)Kbh + (size_t)(tile) * (64 * 384) + doffK[i]), (LAS unsigned*)(lds + (slot) * KT_BYTES + pc * 1024), 16, 0, 0); } } while (0)
; #define ATT_DMAV(tile, slot) do { _Pragma("unroll") for (int i = 0; i < 3; ++i) { const int pc = (wv + 8 * i) < 18 ? (wv + 8 * i) : 17; \
;         __builtin_amdgcn_global_load_lds((const unsigned*)((const char*)Vbh + (size_t)(tile) * 128 + doffV[i]), (LAS unsigned*)(lds + VRING + (slot) * VT_BYTES + pc * 1024), 16, 0, 0); } } while (0)
; __device__ __forceinline__ void attn_unit(const bf16_t* Qrows  , const bf16_t* Kbh, const bf16_t* Vbh, int nkeys, bf16_t* Orows, LAS unsigned char* lds) {
;     ...
;         if (j + 4 < nt) ATT_DMAK(j + 4, v0);
;         if (j + 3 < nt) ATT_DMAV(j + 3, v0 == 0 ? 2 : v0 - 1);
.LBB0_1235:
	s_add_i32 s15, s14, 1
	s_cmp_lg_u32 s14, 2
	s_cselect_b32 s14, s15, 0
	s_mul_i32 s15, s14, 0x6400
	v_add_u32_e32 v70, s15, v185
	ds_read_b128 v[66:69], v70
	ds_read_b128 v[166:169], v70 offset:32
	ds_read_b128 v[170:173], v70 offset:64
	ds_read_b128 v[188:191], v70 offset:96
	ds_read_b128 v[192:195], v70 offset:128
	ds_read_b128 v[196:199], v70 offset:160
	ds_read_b128 v[200:203], v70 offset:192
	ds_read_b128 v[216:219], v70 offset:224
	ds_read_b128 v[220:223], v70 offset:256
	ds_read_b128 v[224:227], v70 offset:288
	ds_read_b128 v[228:231], v70 offset:320
	ds_read_b128 v[146:149], v70 offset:352
	s_waitcnt lgkmcnt(11)
	v_mfma_f32_32x32x16_bf16 v[66:81], v[66:69], v[142:145], 0
	v_sub_f32_e32 v82, v82, v183
	v_exp_f32_e32 v82, v82
	v_sub_f32_e32 v94, v94, v183
	v_exp_f32_e32 v94, v94
	v_add_f32_e32 v165, 0, v82
	v_add_f32_e32 v165, v94, v165
	s_waitcnt lgkmcnt(10)
	v_mfma_f32_32x32x16_bf16 v[66:81], v[166:169], v[138:141], v[66:81]
	v_sub_f32_e32 v83, v83, v183
	v_exp_f32_e32 v83, v83
	v_sub_f32_e32 v95, v95, v183
	v_exp_f32_e32 v95, v95
	v_add_f32_e32 v165, v83, v165
	v_cvt_pk_bf16_f32 v82, v82, v83
	v_add_f32_e32 v165, v95, v165
	v_sub_f32_e32 v83, v84, v183
	s_waitcnt lgkmcnt(9)
	v_mfma_f32_32x32x16_bf16 v[66:81], v[170:173], v[134:137], v[66:81]
	v_exp_f32_e32 v83, v83
	v_sub_f32_e32 v96, v96, v183
	v_add_f32_e32 v84, v83, v165
	v_exp_f32_e32 v165, v96
	s_nop 0
	v_add_f32_e32 v84, v165, v84
	s_waitcnt lgkmcnt(8)
	v_mfma_f32_32x32x16_bf16 v[66:81], v[188:191], v[130:133], v[66:81]
	v_sub_f32_e32 v85, v85, v183
	v_exp_f32_e32 v85, v85
	v_sub_f32_e32 v96, v97, v183
	v_exp_f32_e32 v97, v96
	v_cvt_pk_bf16_f32 v96, v94, v95
	v_add_f32_e32 v84, v85, v84
	v_cvt_pk_bf16_f32 v83, v83, v85
	v_add_f32_e32 v84, v97, v84
	v_cvt_pk_bf16_f32 v97, v165, v97
	s_waitcnt lgkmcnt(7)
	v_mfma_f32_32x32x16_bf16 v[66:81], v[192:195], v[126:129], v[66:81]
	v_sub_f32_e32 v85, v86, v183
	v_exp_f32_e32 v85, v85
	s_nop 0
	v_add_f32_e32 v84, v85, v84
	s_waitcnt lgkmcnt(6)
	v_mfma_f32_32x32x16_bf16 v[66:81], v[196:199], v[122:125], v[66:81]
	v_sub_f32_e32 v86, v87, v183
	v_exp_f32_e32 v86, v86
	s_nop 0
	v_add_f32_e32 v87, v86, v84
	v_cvt_pk_bf16_f32 v84, v85, v86
	s_waitcnt lgkmcnt(5)
	v_mfma_f32_32x32x16_bf16 v[66:81], v[200:203], v[118:121], v[66:81]
	v_sub_f32_e32 v85, v88, v183
	v_exp_f32_e32 v85, v85
	s_nop 0
	v_add_f32_e32 v86, v85, v87
	s_waitcnt lgkmcnt(4)
	v_mfma_f32_32x32x16_bf16 v[66:81], v[216:219], v[114:117], v[66:81]
	v_sub_f32_e32 v87, v89, v183
	v_exp_f32_e32 v87, v87
	s_nop 0
	v_add_f32_e32 v86, v87, v86
	v_cvt_pk_bf16_f32 v85, v85, v87
	v_sub_f32_e32 v87, v90, v183
	v_exp_f32_e32 v90, v87
	s_waitcnt lgkmcnt(3)
	v_mfma_f32_32x32x16_bf16 v[66:81], v[220:223], v[110:113], v[66:81]
	v_add_u32_e32 v165, s13, v187
	v_add_f32_e32 v94, v90, v86
	ds_read_b128 v[86:89], v165
	ds_read_b128 v[166:169], v165 offset:32
	s_waitcnt lgkmcnt(4)
	v_mfma_f32_32x32x16_bf16 v[66:81], v[224:227], v[106:109], v[66:81]
	v_sub_f32_e32 v91, v91, v183
	ds_read_b128 v[170:173], v165 offset:4608
	ds_read_b128 v[188:191], v165 offset:4640
	v_exp_f32_e32 v91, v91
	s_nop 0
	v_add_f32_e32 v95, v91, v94
	v_cvt_pk_bf16_f32 v94, v90, v91
	s_waitcnt lgkmcnt(5)
	v_mfma_f32_32x32x16_bf16 v[66:81], v[228:231], v[102:105], v[66:81]
	v_sub_f32_e32 v90, v92, v183
	ds_read_b128 v[192:195], v165 offset:9216
	ds_read_b128 v[196:199], v165 offset:9248
	v_exp_f32_e32 v90, v90
	s_nop 0
	v_add_f32_e32 v91, v90, v95
	v_sub_f32_e32 v92, v93, v183
	v_exp_f32_e32 v92, v92
	s_waitcnt lgkmcnt(6)
	v_mfma_f32_32x32x16_bf16 v[66:81], v[146:149], v[98:101], v[66:81]
	v_add_f32_e32 v186, v92, v91
	v_cvt_pk_bf16_f32 v95, v90, v92
	ds_read_b128 v[90:93], v165 offset:13824
	ds_read_b128 v[146:149], v165 offset:13856
	s_waitcnt lgkmcnt(0)
	v_mfma_f32_32x32x16_bf16 v[50:65], v[86:89], v[82:85], v[50:65]
	v_add_f32_e32 v186, v164, v186
	v_mfma_f32_32x32x16_bf16 v[34:49], v[170:173], v[82:85], v[34:49]
	s_and_b64 vcc, exec, s[0:1]
	s_cbranch_vccnz .LattB_v
	s_mul_i32 s13, s12, 0x6400
	s_add_i32 s13, s13, 0
	s_add_u32 s16, s80, s2
	s_addc_u32 s17, s81, s3
	s_add_u32 s16, s16, 0x30e90000
	s_addc_u32 s17, s17, 0
	s_add_i32 m0, s13, s65
	s_nop 0
	global_load_lds_dwordx4 v208, s[16:17]
	s_add_i32 m0, s13, s66
	s_nop 0
	global_load_lds_dwordx4 v209, s[16:17]
	s_add_i32 m0, s13, s67
	s_add_i32 s13, s13, s68
	global_load_lds_dwordx4 v210, s[16:17]
	s_add_i32 m0, s13, 0x6000
	s_nop 0
	global_load_lds_dwordx4 v211, s[16:17]
.LattB_v:
	v_mfma_f32_32x32x16_bf16 v[18:33], v[192:195], v[82:85], v[18:33]
	v_max_f32_e32 v150, v66, v67
	v_max3_f32 v150, v150, v68, v69
	v_mfma_f32_32x32x16_bf16 v[2:17], v[90:93], v[82:85], v[2:17]
	v_max3_f32 v150, v150, v70, v71
	v_max3_f32 v150, v150, v72, v73
	v_mfma_f32_32x32x16_bf16 v[50:65], v[166:169], v[94:97], v[50:65]
	s_andn2_b64 vcc, exec, s[24:25]
	s_mul_i32 s13, s12, 0x4800
	s_cbranch_vccnz .LattB_end
	s_add_i32 s15, s13, 0xffffb800
	s_cmp_lg_u32 s12, 0
	s_cselect_b32 s15, s15, 0x9000
	s_add_i32 s15, s15, 0
	s_add_i32 s15, s15, 0x12c00
	s_add_u32 s16, s82, s2
	s_addc_u32 s17, s83, s3
	s_add_u32 s16, s16, 0x31bf8180
	s_addc_u32 s17, s17, 0
	s_add_i32 m0, s15, s69
	s_nop 0
	global_load_lds_dwordx4 v212, s[16:17]
	s_add_i32 m0, s15, s70
	s_nop 0
	global_load_lds_dwordx4 v213, s[16:17]
	s_add_i32 m0, s15, s71
	s_nop 0
	global_load_lds_dwordx4 v214, s[16:17]
.LattB_end:
	v_max3_f32 v150, v150, v74, v75
	v_max3_f32 v150, v150, v76, v77
	v_mfma_f32_32x32x16_bf16 v[34:49], v[188:191], v[94:97], v[34:49]
	v_max3_f32 v150, v150, v78, v79
	v_max3_f32 v150, v150, v80, v81
	v_mfma_f32_32x32x16_bf16 v[18:33], v[196:199], v[94:97], v[18:33]
	v_mfma_f32_32x32x16_bf16 v[2:17], v[146:149], v[94:97], v[2:17]
	v_mov_b32_e32 v151, v150
	s_nop 1
	v_permlane32_swap_b32_e32 v151, v150
	v_max_f32_e32 v150, v150, v151
	s_add_i32 s13, s14, 1
	s_cmp_lg_u32 s14, 2
	s_cselect_b32 s14, s13, 0
	s_add_i32 s13, s12, 1
	s_cmp_lg_u32 s12, 2
	s_cselect_b32 s36, s13, 0
	s_add_u32 s80, s80, s6
	s_addc_u32 s81, s81, s7
	s_add_u32 s82, s82, s10
	s_addc_u32 s83, s83, s11
	s_add_i32 s63, s63, 2
	s_andn2_b64 vcc, exec, s[0:1]
	s_cbranch_vccz .LBB0_1250

; #define ATT_DMAK(tile, slot) do { _Pragma("unroll") for (int i = 0; i < 4; ++i) { const int pc = (wv + 8 * i) < 25 ? (wv + 8 * i) : 24; \
;         __builtin_amdgcn_global_load_lds((const unsigned*)((const char*)Kbh + (size_t)(tile) * (64 * 384) + doffK[i]), (LAS unsigned*)(lds + (slot) * KT_BYTES + pc * 1024), 16, 0, 0); } } while (0)
; #define ATT_DMAV(tile, slot) do { _Pragma("unroll") for (int i = 0; i < 3; ++i) { const int pc = (wv + 8 * i) < 18 ? (wv + 8 * i) : 17; \
;         __builtin_amdgcn_global_load_lds((const unsigned*)((const char*)Vbh + (size_t)(tile) * 128 + doffV[i]), (LAS unsigned*)(lds + VRING + (slot) * VT_BYTES + pc * 1024), 16, 0, 0); } } while (0)
; __device__ __forceinline__ void attn_unit(const bf16_t* Qrows  , const bf16_t* Kbh, const bf16_t* Vbh, int nkeys, bf16_t* Orows, LAS unsigned char* lds) {
;     ...
;         if (j + 3 < nt) ATT_DMAK(j + 3, v0);
;         ATT_DMAV(j + 2, v0 == 0 ? 2 : v0 - 1);
.LBB0_1240:
	s_mul_i32 s13, s14, 0x6400
	v_add_u32_e32 v86, s13, v185
	ds_read_b128 v[82:85], v86
	ds_read_b128 v[188:191], v86 offset:32
	ds_read_b128 v[192:195], v86 offset:64
	ds_read_b128 v[196:199], v86 offset:96
	ds_read_b128 v[200:203], v86 offset:128
	ds_read_b128 v[216:219], v86 offset:160
	ds_read_b128 v[220:223], v86 offset:192
	ds_read_b128 v[224:227], v86 offset:224
	ds_read_b128 v[228:231], v86 offset:256
	ds_read_b128 v[232:235], v86 offset:288
	ds_read_b128 v[236:239], v86 offset:320
	ds_read_b128 v[240:243], v86 offset:352
	s_waitcnt lgkmcnt(11)
	v_mfma_f32_32x32x16_bf16 v[82:97], v[82:85], v[142:145], 0
	v_sub_f32_e32 v66, v66, v183
	v_sub_f32_e32 v78, v78, v183
	v_exp_f32_e32 v66, v66
	v_exp_f32_e32 v78, v78
	s_waitcnt lgkmcnt(10)
	v_mfma_f32_32x32x16_bf16 v[82:97], v[188:191], v[138:141], v[82:97]
	v_sub_f32_e32 v67, v67, v183
	v_sub_f32_e32 v79, v79, v183
	v_exp_f32_e32 v67, v67
	v_exp_f32_e32 v79, v79
	v_cvt_pk_bf16_f32 v188, v66, v67
	s_waitcnt lgkmcnt(9)
	v_mfma_f32_32x32x16_bf16 v[82:97], v[192:195], v[134:137], v[82:97]
	v_sub_f32_e32 v68, v68, v183
	v_sub_f32_e32 v80, v80, v183
	v_exp_f32_e32 v68, v68
	v_exp_f32_e32 v80, v80
	s_waitcnt lgkmcnt(8)
	v_mfma_f32_32x32x16_bf16 v[82:97], v[196:199], v[130:133], v[82:97]
	v_sub_f32_e32 v69, v69, v183
	v_sub_f32_e32 v81, v81, v183
	v_exp_f32_e32 v69, v69
	v_exp_f32_e32 v81, v81
	v_cvt_pk_bf16_f32 v194, v78, v79
	v_cvt_pk_bf16_f32 v189, v68, v69
	v_cvt_pk_bf16_f32 v195, v80, v81
	s_waitcnt lgkmcnt(7)
	v_mfma_f32_32x32x16_bf16 v[82:97], v[200:203], v[126:129], v[82:97]
	v_sub_f32_e32 v70, v70, v183
	v_exp_f32_e32 v70, v70
	s_waitcnt lgkmcnt(6)
	v_mfma_f32_32x32x16_bf16 v[82:97], v[216:219], v[122:125], v[82:97]
	v_sub_f32_e32 v71, v71, v183
	v_exp_f32_e32 v71, v71
	s_nop 0
	v_cvt_pk_bf16_f32 v190, v70, v71
	s_waitcnt lgkmcnt(5)
	v_mfma_f32_32x32x16_bf16 v[82:97], v[220:223], v[118:121], v[82:97]
	v_sub_f32_e32 v72, v72, v183
	v_exp_f32_e32 v72, v72
	s_waitcnt lgkmcnt(4)
	v_mfma_f32_32x32x16_bf16 v[82:97], v[224:227], v[114:117], v[82:97]
	v_sub_f32_e32 v73, v73, v183
	v_exp_f32_e32 v73, v73
	s_nop 0
	v_cvt_pk_bf16_f32 v191, v72, v73
	s_waitcnt lgkmcnt(3)
	v_mfma_f32_32x32x16_bf16 v[82:97], v[228:231], v[110:113], v[82:97]
	v_add_u32_e32 v204, s12, v187
	v_sub_f32_e32 v74, v74, v183
	ds_read_b128 v[196:199], v204
	ds_read_b128 v[200:203], v204 offset:32
	v_exp_f32_e32 v74, v74
	s_waitcnt lgkmcnt(4)
	v_mfma_f32_32x32x16_bf16 v[82:97], v[232:235], v[106:109], v[82:97]
	v_sub_f32_e32 v75, v75, v183
	ds_read_b128 v[216:219], v204 offset:4608
	ds_read_b128 v[220:223], v204 offset:4640
	v_exp_f32_e32 v75, v75
	s_nop 0
	v_cvt_pk_bf16_f32 v192, v74, v75
	s_waitcnt lgkmcnt(5)
	v_mfma_f32_32x32x16_bf16 v[82:97], v[236:239], v[102:105], v[82:97]
	v_sub_f32_e32 v76, v76, v183
	ds_read_b128 v[224:227], v204 offset:9216
	ds_read_b128 v[228:231], v204 offset:9248
	v_exp_f32_e32 v76, v76
	s_waitcnt lgkmcnt(6)
	v_mfma_f32_32x32x16_bf16 v[82:97], v[240:243], v[98:101], v[82:97]
	v_sub_f32_e32 v77, v77, v183
	ds_read_b128 v[232:235], v204 offset:13824
	ds_read_b128 v[236:239], v204 offset:13856
	v_exp_f32_e32 v77, v77
	s_nop 0
	v_cvt_pk_bf16_f32 v193, v76, v77
	s_waitcnt lgkmcnt(0)
	v_mfma_f32_32x32x16_bf16 v[50:65], v[196:199], v[188:191], v[50:65]
	v_mfma_f32_32x32x16_bf16 v[34:49], v[216:219], v[188:191], v[34:49]
	s_and_b64 vcc, exec, s[0:1]
	s_cbranch_vccnz .LattA_v
	s_mul_i32 s12, s36, 0x6400
	s_add_i32 s12, s12, 0
	s_add_u32 s16, s80, s2
	s_addc_u32 s17, s81, s3
	s_add_u32 s16, s16, 0x30e8a000
	s_addc_u32 s17, s17, 0
	s_add_i32 m0, s12, s65
	s_nop 0
	global_load_lds_dwordx4 v208, s[16:17]
	s_add_i32 m0, s12, s66
	s_nop 0
	global_load_lds_dwordx4 v209, s[16:17]
	s_add_i32 m0, s12, s67
	s_add_i32 s12, s12, s68
	global_load_lds_dwordx4 v210, s[16:17]
	s_add_i32 m0, s12, 0x6000
	s_nop 0
	global_load_lds_dwordx4 v211, s[16:17]
.LattA_v:
	v_mfma_f32_32x32x16_bf16 v[18:33], v[224:227], v[188:191], v[18:33]
	v_max_f32_e32 v152, v82, v83
	v_max3_f32 v152, v152, v84, v85
	v_mfma_f32_32x32x16_bf16 v[2:17], v[232:235], v[188:191], v[2:17]
	v_max3_f32 v152, v152, v86, v87
	v_max3_f32 v152, v152, v88, v89
	v_mfma_f32_32x32x16_bf16 v[50:65], v[200:203], v[192:195], v[50:65]
	s_mul_i32 s12, s36, 0x4800
	s_add_i32 s13, s12, 0xffffb800
	s_cmp_lg_u32 s36, 0
	s_cselect_b32 s13, s13, 0x9000
	s_add_i32 s13, s13, 0
	s_add_i32 s13, s13, 0x12c00
	s_add_u32 s16, s82, s2
	s_addc_u32 s17, s83, s3
	s_add_u32 s16, s16, s28
	s_addc_u32 s17, s17, s29
	s_add_i32 m0, s13, s69
	s_nop 0
	global_load_lds_dwordx4 v212, s[16:17]
	s_add_i32 m0, s13, s70
	s_nop 0
	global_load_lds_dwordx4 v213, s[16:17]
	s_add_i32 m0, s13, s71
	s_nop 0
	global_load_lds_dwordx4 v214, s[16:17]
	v_max3_f32 v152, v152, v90, v91
	v_max3_f32 v152, v152, v92, v93
	v_mfma_f32_32x32x16_bf16 v[34:49], v[220:223], v[192:195], v[34:49]
	v_max3_f32 v152, v152, v94, v95
	v_max3_f32 v152, v152, v96, v97
	v_mfma_f32_32x32x16_bf16 v[18:33], v[228:231], v[192:195], v[18:33]
	v_mfma_f32_32x32x16_bf16 v[2:17], v[236:239], v[192:195], v[2:17]
	v_mov_b32_e32 v153, v152
	s_nop 1
	v_permlane32_swap_b32_e32 v153, v152
	v_max_f32_e32 v152, v152, v153
	s_mov_b64 s[12:13], -1
	s_and_b64 vcc, exec, s[0:1]
	s_cbranch_vccz .LBB0_1242
	s_waitcnt vmcnt(0)
	s_mov_b64 s[12:13], 0
